# shadow workgroups (idle ~15 us at the barrier after the scan phase) pull their own P4 z rows (128 KB each) into L2 from wave 3
# speedup vs baseline: 1.0075x; 1.0075x over previous
.Lcwarm_3:
	s_cmp_lg_u32 s4, 0xc0
	s_cbranch_scc1 .Lzwarm_done
	s_cmp_lt_u32 s94, 0x200
	s_cbranch_scc1 .Lzwarm_done
	s_and_b32 s4, s94, -8
	s_lshl_b32 s4, s4, 10
	s_add_u32 s4, s4, 0x10400000
	s_add_u32 s4, s88, s4
	s_addc_u32 s5, s89, 0
	v_mbcnt_lo_u32_b32 v0, -1, 0
	v_mbcnt_hi_u32_b32 v0, -1, v0
	v_lshlrev_b32_e32 v0, 7, v0
	global_load_dword v1, v0, s[4:5]
	s_add_u32 s4, s4, 0x200000
	s_addc_u32 s5, s5, 0
	global_load_dword v1, v0, s[4:5]
	s_add_u32 s4, s4, 0x200000
	s_addc_u32 s5, s5, 0
	global_load_dword v1, v0, s[4:5]
	s_add_u32 s4, s4, 0x200000
	s_addc_u32 s5, s5, 0
	global_load_dword v1, v0, s[4:5]
	s_add_u32 s4, s4, 0x200000
	s_addc_u32 s5, s5, 0
	global_load_dword v1, v0, s[4:5]
	s_add_u32 s4, s4, 0x200000
	s_addc_u32 s5, s5, 0
	global_load_dword v1, v0, s[4:5]
	s_add_u32 s4, s4, 0x200000
	s_addc_u32 s5, s5, 0
	global_load_dword v1, v0, s[4:5]
	s_add_u32 s4, s4, 0x200000
	s_addc_u32 s5, s5, 0
	global_load_dword v1, v0, s[4:5]
	s_add_u32 s4, s4, 0x200000
	s_addc_u32 s5, s5, 0
	global_load_dword v1, v0, s[4:5]
	s_add_u32 s4, s4, 0x200000
	s_addc_u32 s5, s5, 0
	global_load_dword v1, v0, s[4:5]
	s_add_u32 s4, s4, 0x200000
	s_addc_u32 s5, s5, 0
	global_load_dword v1, v0, s[4:5]
	s_add_u32 s4, s4, 0x200000
	s_addc_u32 s5, s5, 0
	global_load_dword v1, v0, s[4:5]
	s_add_u32 s4, s4, 0x200000
	s_addc_u32 s5, s5, 0
	global_load_dword v1, v0, s[4:5]
	s_add_u32 s4, s4, 0x200000
	s_addc_u32 s5, s5, 0
	global_load_dword v1, v0, s[4:5]
	s_add_u32 s4, s4, 0x200000
	s_addc_u32 s5, s5, 0
	global_load_dword v1, v0, s[4:5]
	s_add_u32 s4, s4, 0x200000
	s_addc_u32 s5, s5, 0
	global_load_dword v1, v0, s[4:5]
	s_waitcnt vmcnt(0)
